# metadata register counts brought in line with the descriptors (no code change since v39)
# speedup vs baseline: 1.0011x; 1.0011x over previous
amdhsa.kernels:
  - .agpr_count:     0
    .args:
      - .actual_access:  read_only
        .address_space:  global
        .offset:         0
        .size:           8
        .value_kind:     global_buffer
      - .actual_access:  read_only
        .address_space:  global
        .offset:         8
        .size:           8
        .value_kind:     global_buffer
      - .actual_access:  read_only
        .address_space:  global
        .offset:         16
        .size:           8
        .value_kind:     global_buffer
      - .actual_access:  read_only
        .address_space:  global
        .offset:         24
        .size:           8
        .value_kind:     global_buffer
      - .actual_access:  read_only
        .address_space:  global
        .offset:         32
        .size:           8
        .value_kind:     global_buffer
      - .actual_access:  write_only
        .address_space:  global
        .offset:         40
        .size:           8
        .value_kind:     global_buffer
      - .actual_access:  write_only
        .address_space:  global
        .offset:         48
        .size:           8
        .value_kind:     global_buffer
      - .actual_access:  write_only
        .address_space:  global
        .offset:         56
        .size:           8
        .value_kind:     global_buffer
      - .actual_access:  write_only
        .address_space:  global
        .offset:         64
        .size:           8
        .value_kind:     global_buffer
      - .actual_access:  write_only
        .address_space:  global
        .offset:         72
        .size:           8
        .value_kind:     global_buffer
      - .actual_access:  write_only
        .address_space:  global
        .offset:         80
        .size:           8
        .value_kind:     global_buffer
      - .actual_access:  write_only
        .address_space:  global
        .offset:         88
        .size:           8
        .value_kind:     global_buffer
      - .actual_access:  read_only
        .address_space:  global
        .offset:         96
        .size:           8
        .value_kind:     global_buffer
      - .actual_access:  write_only
        .address_space:  global
        .offset:         104
        .size:           8
        .value_kind:     global_buffer
    .group_segment_fixed_size: 16624
    .kernarg_segment_align: 8
    .kernarg_segment_size: 112
    .language:       OpenCL C
    .language_version:
      - 2
      - 0
    .max_flat_workgroup_size: 256
    .name:           _Z6k_prepPKiPKfS2_S2_S2_PjPiP15HIP_vector_typeIjLj4EES7_S7_PfS4_S2_PS5_IjLj2EE
    .private_segment_fixed_size: 0
    .sgpr_count:     42
    .sgpr_spill_count: 0
    .symbol:         _Z6k_prepPKiPKfS2_S2_S2_PjPiP15HIP_vector_typeIjLj4EES7_S7_PfS4_S2_PS5_IjLj2EE.kd
    .uniform_work_group_size: 1
    .uses_dynamic_stack: false
    .vgpr_count:     55
    .vgpr_spill_count: 0
    .wavefront_size: 64
  - .agpr_count:     0
    .args:
      - .actual_access:  read_only
        .address_space:  global
        .offset:         0
        .size:           8
        .value_kind:     global_buffer
      - .actual_access:  read_only
        .address_space:  global
        .offset:         8
        .size:           8
        .value_kind:     global_buffer
      - .address_space:  global
        .offset:         16
        .size:           8
        .value_kind:     global_buffer
      - .address_space:  global
        .offset:         24
        .size:           8
        .value_kind:     global_buffer
      - .actual_access:  write_only
        .address_space:  global
        .offset:         32
        .size:           8
        .value_kind:     global_buffer
      - .actual_access:  read_only
        .address_space:  global
        .offset:         40
        .size:           8
        .value_kind:     global_buffer
      - .actual_access:  write_only
        .address_space:  global
        .offset:         48
        .size:           8
        .value_kind:     global_buffer
      - .actual_access:  write_only
        .address_space:  global
        .offset:         56
        .size:           8
        .value_kind:     global_buffer
    .group_segment_fixed_size: 25136
    .kernarg_segment_align: 8
    .kernarg_segment_size: 64
    .language:       OpenCL C
    .language_version:
      - 2
      - 0
    .max_flat_workgroup_size: 512
    .name:           _Z10k_csr_agg1PKjPKiPiPtPjPK15HIP_vector_typeIjLj2EEPS7_SA_
    .private_segment_fixed_size: 0
    .sgpr_count:     66
    .sgpr_spill_count: 0
    .symbol:         _Z10k_csr_agg1PKjPKiPiPtPjPK15HIP_vector_typeIjLj2EEPS7_SA_.kd
    .uniform_work_group_size: 1
    .uses_dynamic_stack: false
    .vgpr_count:     64
    .vgpr_spill_count: 0
    .wavefront_size: 64
  - .agpr_count:     0
    .args:
      - .actual_access:  read_only
        .address_space:  global
        .offset:         0
        .size:           8
        .value_kind:     global_buffer
      - .actual_access:  read_only
        .address_space:  global
        .offset:         8
        .size:           8
        .value_kind:     global_buffer
      - .address_space:  global
        .offset:         16
        .size:           8
        .value_kind:     global_buffer
      - .address_space:  global
        .offset:         24
        .size:           8
        .value_kind:     global_buffer
      - .actual_access:  read_only
        .address_space:  global
        .offset:         32
        .size:           8
        .value_kind:     global_buffer
      - .actual_access:  read_only
        .address_space:  global
        .offset:         40
        .size:           8
        .value_kind:     global_buffer
      - .actual_access:  read_only
        .address_space:  global
        .offset:         48
        .size:           8
        .value_kind:     global_buffer
      - .actual_access:  write_only
        .address_space:  global
        .offset:         56
        .size:           8
        .value_kind:     global_buffer
      - .actual_access:  write_only
        .address_space:  global
        .offset:         64
        .size:           8
        .value_kind:     global_buffer
      - .offset:         72
        .size:           4
        .value_kind:     hidden_block_count_x
      - .offset:         76
        .size:           4
        .value_kind:     hidden_block_count_y
      - .offset:         80
        .size:           4
        .value_kind:     hidden_block_count_z
      - .offset:         84
        .size:           2
        .value_kind:     hidden_group_size_x
      - .offset:         86
        .size:           2
        .value_kind:     hidden_group_size_y
      - .offset:         88
        .size:           2
        .value_kind:     hidden_group_size_z
      - .offset:         90
        .size:           2
        .value_kind:     hidden_remainder_x
      - .offset:         92
        .size:           2
        .value_kind:     hidden_remainder_y
      - .offset:         94
        .size:           2
        .value_kind:     hidden_remainder_z
      - .offset:         112
        .size:           8
        .value_kind:     hidden_global_offset_x
      - .offset:         120
        .size:           8
        .value_kind:     hidden_global_offset_y
      - .offset:         128
        .size:           8
        .value_kind:     hidden_global_offset_z
      - .offset:         136
        .size:           2
        .value_kind:     hidden_grid_dims
    .group_segment_fixed_size: 76544
    .kernarg_segment_align: 8
    .kernarg_segment_size: 328
    .language:       OpenCL C
    .language_version:
      - 2
      - 0
    .max_flat_workgroup_size: 512
    .name:           _Z6k_gemmPK15HIP_vector_typeIjLj4EES2_PKS_IjLj2EES5_PKfS7_S7_PjS8_
    .private_segment_fixed_size: 0
    .sgpr_count:     54
    .sgpr_spill_count: 0
    .symbol:         _Z6k_gemmPK15HIP_vector_typeIjLj4EES2_PKS_IjLj2EES5_PKfS7_S7_PjS8_.kd
    .uniform_work_group_size: 1
    .uses_dynamic_stack: false
    .vgpr_count:     124
    .vgpr_spill_count: 0
    .wavefront_size: 64
  - .agpr_count:     0
    .args:
      - .actual_access:  read_only
        .address_space:  global
        .offset:         0
        .size:           8
        .value_kind:     global_buffer
      - .actual_access:  read_only
        .address_space:  global
        .offset:         8
        .size:           8
        .value_kind:     global_buffer
      - .actual_access:  read_only
        .address_space:  global
        .offset:         16
        .size:           8
        .value_kind:     global_buffer
      - .actual_access:  read_only
        .address_space:  global
        .offset:         24
        .size:           8
        .value_kind:     global_buffer
      - .actual_access:  write_only
        .address_space:  global
        .offset:         32
        .size:           8
        .value_kind:     global_buffer
    .group_segment_fixed_size: 0
    .kernarg_segment_align: 8
    .kernarg_segment_size: 40
    .language:       OpenCL C
    .language_version:
      - 2
      - 0
    .max_flat_workgroup_size: 256
    .name:           _Z6k_agg2PK15HIP_vector_typeIjLj2EEPKS_IjLj4EEPKtPKjPf
    .private_segment_fixed_size: 0
    .sgpr_count:     19
    .sgpr_spill_count: 0
    .symbol:         _Z6k_agg2PK15HIP_vector_typeIjLj2EEPKS_IjLj4EEPKtPKjPf.kd
    .uniform_work_group_size: 1
    .uses_dynamic_stack: false
    .vgpr_count:     64
    .vgpr_spill_count: 0
    .wavefront_size: 64
